# k0 K-loop: six SP2 staging LDS-DMA loads issued inside the MFMA block (interleaved) instead of the load part; SP2 waits re-derived vmcnt 8->2, relaxed 24->18
# baseline (speedup 1.0000x reference)
.LBB0_200:
	s_waitcnt lgkmcnt(0)
	s_barrier
	s_setprio 1
	s_waitcnt lgkmcnt(0)
	v_mfma_f32_16x16x32_bf16 v[72:75], v[156:159], v[196:199], v[72:75]
	v_mfma_f32_16x16x32_bf16 v[68:71], v[164:167], v[196:199], v[68:71]
	s_mov_b32 m0, s86
	v_mfma_f32_16x16x32_bf16 v[54:57], v[156:159], v[188:191], v[54:57]
	v_mfma_f32_16x16x32_bf16 v[50:53], v[164:167], v[188:191], v[50:53]
	global_load_lds_dwordx4 v[234:235], off
	s_mov_b32 m0, s87
	v_mfma_f32_16x16x32_bf16 v[38:41], v[156:159], v[180:183], v[38:41]
	v_mfma_f32_16x16x32_bf16 v[34:37], v[164:167], v[180:183], v[34:37]
	global_load_lds_dwordx4 v[232:233], off
	v_lshl_add_u64 v[228:229], s[8:9], 0, v[210:211]
	s_mov_b32 m0, s88
	v_mfma_f32_16x16x32_bf16 v[22:25], v[156:159], v[172:175], v[22:25]
	v_mfma_f32_16x16x32_bf16 v[18:21], v[164:167], v[172:175], v[18:21]
	global_load_lds_dwordx4 v[228:229], off
	v_lshl_add_u64 v[228:229], s[8:9], 0, v[214:215]
	s_mov_b32 m0, s89
	v_mfma_f32_16x16x32_bf16 v[72:75], v[160:163], v[200:203], v[72:75]
	v_mfma_f32_16x16x32_bf16 v[68:71], v[168:171], v[200:203], v[68:71]
	global_load_lds_dwordx4 v[228:229], off
	v_lshl_add_u64 v[228:229], s[58:59], 0, v[208:209]
	s_mov_b32 m0, s85
	v_mfma_f32_16x16x32_bf16 v[54:57], v[160:163], v[192:195], v[54:57]
	v_mfma_f32_16x16x32_bf16 v[50:53], v[168:171], v[192:195], v[50:53]
	global_load_lds_dwordx4 v[228:229], off
	s_mov_b32 m0, s90
	v_mfma_f32_16x16x32_bf16 v[38:41], v[160:163], v[184:187], v[38:41]
	v_mfma_f32_16x16x32_bf16 v[34:37], v[168:171], v[184:187], v[34:37]
	global_load_lds_dwordx4 v[230:231], off
	v_mfma_f32_16x16x32_bf16 v[22:25], v[160:163], v[176:179], v[22:25]
	v_mfma_f32_16x16x32_bf16 v[18:21], v[168:171], v[176:179], v[18:21]
	v_mfma_f32_16x16x32_bf16 v[62:65], v[140:143], v[196:199], v[62:65]
	v_mfma_f32_16x16x32_bf16 v[58:61], v[148:151], v[196:199], v[58:61]
	v_mfma_f32_16x16x32_bf16 v[46:49], v[140:143], v[188:191], v[46:49]
	v_mfma_f32_16x16x32_bf16 v[42:45], v[148:151], v[188:191], v[42:45]
	v_mfma_f32_16x16x32_bf16 v[30:33], v[140:143], v[180:183], v[30:33]
	v_mfma_f32_16x16x32_bf16 v[26:29], v[148:151], v[180:183], v[26:29]
	v_mfma_f32_16x16x32_bf16 v[14:17], v[140:143], v[172:175], v[14:17]
	v_mfma_f32_16x16x32_bf16 v[10:13], v[148:151], v[172:175], v[10:13]
	v_mfma_f32_16x16x32_bf16 v[62:65], v[144:147], v[200:203], v[62:65]
	v_mfma_f32_16x16x32_bf16 v[58:61], v[152:155], v[200:203], v[58:61]
	v_mfma_f32_16x16x32_bf16 v[46:49], v[144:147], v[192:195], v[46:49]
	v_mfma_f32_16x16x32_bf16 v[42:45], v[152:155], v[192:195], v[42:45]
	v_mfma_f32_16x16x32_bf16 v[30:33], v[144:147], v[184:187], v[30:33]
	v_mfma_f32_16x16x32_bf16 v[26:29], v[152:155], v[184:187], v[26:29]
	v_mfma_f32_16x16x32_bf16 v[14:17], v[144:147], v[176:179], v[14:17]
	v_mfma_f32_16x16x32_bf16 v[10:13], v[152:155], v[176:179], v[10:13]
	s_setprio 0
	s_barrier
	s_add_i32 s10, 0, 0x18000
	v_add_u32_e32 v66, s10, v219
	s_add_i32 s11, 0, 0x1c000
	ds_read_b128 v[140:143], v66
	ds_read_b128 v[144:147], v66 offset:1024
	ds_read_b128 v[148:151], v66 offset:2048
	ds_read_b128 v[152:155], v66 offset:3072
	v_add_u32_e32 v66, s11, v219
	ds_read_b128 v[156:159], v66
	ds_read_b128 v[160:163], v66 offset:1024
	ds_read_b128 v[164:167], v66 offset:2048
	ds_read_b128 v[168:171], v66 offset:3072
	s_add_u32 s8, s58, 0x40000
	s_addc_u32 s9, s59, 0
	s_mov_b32 m0, s91
	v_lshl_add_u64 v[246:247], s[8:9], 0, v[208:209]
	ds_read_b128 v[172:175], v244 offset:32768
	ds_read_b128 v[176:179], v244 offset:33792
	ds_read_b128 v[180:183], v244 offset:34816
	ds_read_b128 v[184:187], v244 offset:35840
	ds_read_b128 v[188:191], v244 offset:36864
	ds_read_b128 v[192:195], v244 offset:37888
	ds_read_b128 v[196:199], v244 offset:38912
	ds_read_b128 v[200:203], v244 offset:39936
	global_load_lds_dwordx4 v[246:247], off
	v_lshl_add_u64 v[246:247], s[8:9], 0, v[212:213]
	s_mov_b32 m0, s92
	s_nop 0
	global_load_lds_dwordx4 v[246:247], off
	s_waitcnt vmcnt(8)
	s_waitcnt lgkmcnt(0)
	s_barrier
	s_setprio 1
	s_waitcnt lgkmcnt(0)
	v_mfma_f32_16x16x32_bf16 v[136:139], v[140:143], v[172:175], v[136:139]
	v_mfma_f32_16x16x32_bf16 v[132:135], v[148:151], v[172:175], v[132:135]
	v_mfma_f32_16x16x32_bf16 v[120:123], v[140:143], v[180:183], v[120:123]
	v_mfma_f32_16x16x32_bf16 v[116:119], v[148:151], v[180:183], v[116:119]
	v_mfma_f32_16x16x32_bf16 v[104:107], v[140:143], v[188:191], v[104:107]
	v_mfma_f32_16x16x32_bf16 v[100:103], v[148:151], v[188:191], v[100:103]
	v_mfma_f32_16x16x32_bf16 v[88:91], v[140:143], v[196:199], v[88:91]
	v_mfma_f32_16x16x32_bf16 v[84:87], v[148:151], v[196:199], v[84:87]
	v_mfma_f32_16x16x32_bf16 v[136:139], v[144:147], v[176:179], v[136:139]
	v_mfma_f32_16x16x32_bf16 v[132:135], v[152:155], v[176:179], v[132:135]
	v_mfma_f32_16x16x32_bf16 v[120:123], v[144:147], v[184:187], v[120:123]
	v_mfma_f32_16x16x32_bf16 v[116:119], v[152:155], v[184:187], v[116:119]
	v_mfma_f32_16x16x32_bf16 v[104:107], v[144:147], v[192:195], v[104:107]
	v_mfma_f32_16x16x32_bf16 v[100:103], v[152:155], v[192:195], v[100:103]
	v_mfma_f32_16x16x32_bf16 v[88:91], v[144:147], v[200:203], v[88:91]
	v_mfma_f32_16x16x32_bf16 v[84:87], v[152:155], v[200:203], v[84:87]
	s_setprio 0
	s_setprio 1
	v_mfma_f32_16x16x32_bf16 v[128:131], v[156:159], v[172:175], v[128:131]
	v_mfma_f32_16x16x32_bf16 v[124:127], v[164:167], v[172:175], v[124:127]
	v_mfma_f32_16x16x32_bf16 v[112:115], v[156:159], v[180:183], v[112:115]
	v_mfma_f32_16x16x32_bf16 v[108:111], v[164:167], v[180:183], v[108:111]
	v_mfma_f32_16x16x32_bf16 v[96:99], v[156:159], v[188:191], v[96:99]
	v_mfma_f32_16x16x32_bf16 v[92:95], v[164:167], v[188:191], v[92:95]
	v_mfma_f32_16x16x32_bf16 v[80:83], v[156:159], v[196:199], v[80:83]
	v_mfma_f32_16x16x32_bf16 v[76:79], v[164:167], v[196:199], v[76:79]
	v_mfma_f32_16x16x32_bf16 v[128:131], v[160:163], v[176:179], v[128:131]
	v_mfma_f32_16x16x32_bf16 v[124:127], v[168:171], v[176:179], v[124:127]
	v_mfma_f32_16x16x32_bf16 v[112:115], v[160:163], v[184:187], v[112:115]
	v_mfma_f32_16x16x32_bf16 v[108:111], v[168:171], v[184:187], v[108:111]
	v_mfma_f32_16x16x32_bf16 v[96:99], v[160:163], v[192:195], v[96:99]
	v_mfma_f32_16x16x32_bf16 v[92:95], v[168:171], v[192:195], v[92:95]
	v_mfma_f32_16x16x32_bf16 v[80:83], v[160:163], v[200:203], v[80:83]
	v_mfma_f32_16x16x32_bf16 v[76:79], v[168:171], v[200:203], v[76:79]
	s_setprio 0
	s_barrier
	s_add_i32 s12, s10, s84
	v_lshl_add_u64 v[234:235], v[234:235], 0, s[60:61]
	ds_read_b128 v[172:175], v244 offset:49152
	ds_read_b128 v[176:179], v244 offset:50176
	ds_read_b128 v[180:183], v244 offset:51200
	ds_read_b128 v[184:187], v244 offset:52224
	ds_read_b128 v[188:191], v244 offset:53248
	ds_read_b128 v[192:195], v244 offset:54272
	ds_read_b128 v[196:199], v244 offset:55296
	ds_read_b128 v[200:203], v244 offset:56320
	s_add_u32 s8, s36, 0x40080
	v_lshl_add_u64 v[232:233], v[232:233], 0, s[60:61]
	s_addc_u32 s9, s37, 0
	s_add_i32 s10, s11, s84
	s_waitcnt vmcnt(2)
	s_waitcnt lgkmcnt(0)
	s_barrier
	s_setprio 1
	s_waitcnt lgkmcnt(0)
	v_mfma_f32_16x16x32_bf16 v[72:75], v[140:143], v[172:175], v[72:75]
	v_mfma_f32_16x16x32_bf16 v[68:71], v[148:151], v[172:175], v[68:71]
	s_mov_b32 m0, s12
	v_mfma_f32_16x16x32_bf16 v[54:57], v[140:143], v[180:183], v[54:57]
	v_mfma_f32_16x16x32_bf16 v[50:53], v[148:151], v[180:183], v[50:53]
	global_load_lds_dwordx4 v[234:235], off
	s_add_i32 m0, s12, 0x2000
	v_mfma_f32_16x16x32_bf16 v[38:41], v[140:143], v[188:191], v[38:41]
	v_mfma_f32_16x16x32_bf16 v[34:37], v[148:151], v[188:191], v[34:37]
	global_load_lds_dwordx4 v[232:233], off
	v_lshl_add_u64 v[232:233], s[8:9], 0, v[210:211]
	s_mov_b32 m0, s10
	v_mfma_f32_16x16x32_bf16 v[22:25], v[140:143], v[196:199], v[22:25]
	v_mfma_f32_16x16x32_bf16 v[18:21], v[148:151], v[196:199], v[18:21]
	global_load_lds_dwordx4 v[232:233], off
	v_lshl_add_u64 v[232:233], s[8:9], 0, v[214:215]
	s_add_i32 m0, s10, 0x2000
	v_mfma_f32_16x16x32_bf16 v[72:75], v[144:147], v[176:179], v[72:75]
	v_mfma_f32_16x16x32_bf16 v[68:71], v[152:155], v[176:179], v[68:71]
	global_load_lds_dwordx4 v[232:233], off
	v_lshl_add_u64 v[228:229], v[228:229], 0, s[60:61]
	s_mov_b32 m0, s96
	v_mfma_f32_16x16x32_bf16 v[54:57], v[144:147], v[184:187], v[54:57]
	v_mfma_f32_16x16x32_bf16 v[50:53], v[152:155], v[184:187], v[50:53]
	global_load_lds_dwordx4 v[228:229], off
	v_lshl_add_u64 v[228:229], v[230:231], 0, s[60:61]
	s_mov_b32 m0, s97
	v_mfma_f32_16x16x32_bf16 v[38:41], v[144:147], v[192:195], v[38:41]
	v_mfma_f32_16x16x32_bf16 v[34:37], v[152:155], v[192:195], v[34:37]
	global_load_lds_dwordx4 v[228:229], off
	v_mfma_f32_16x16x32_bf16 v[22:25], v[144:147], v[200:203], v[22:25]
	v_mfma_f32_16x16x32_bf16 v[18:21], v[152:155], v[200:203], v[18:21]
	v_mfma_f32_16x16x32_bf16 v[62:65], v[156:159], v[172:175], v[62:65]
	v_mfma_f32_16x16x32_bf16 v[58:61], v[164:167], v[172:175], v[58:61]
	v_mfma_f32_16x16x32_bf16 v[46:49], v[156:159], v[180:183], v[46:49]
	v_mfma_f32_16x16x32_bf16 v[42:45], v[164:167], v[180:183], v[42:45]
	v_mfma_f32_16x16x32_bf16 v[30:33], v[156:159], v[188:191], v[30:33]
	v_mfma_f32_16x16x32_bf16 v[26:29], v[164:167], v[188:191], v[26:29]
	v_mfma_f32_16x16x32_bf16 v[14:17], v[156:159], v[196:199], v[14:17]
	v_mfma_f32_16x16x32_bf16 v[10:13], v[164:167], v[196:199], v[10:13]
	v_mfma_f32_16x16x32_bf16 v[62:65], v[160:163], v[176:179], v[62:65]
	v_mfma_f32_16x16x32_bf16 v[58:61], v[168:171], v[176:179], v[58:61]
	v_mfma_f32_16x16x32_bf16 v[46:49], v[160:163], v[184:187], v[46:49]
	v_mfma_f32_16x16x32_bf16 v[42:45], v[168:171], v[184:187], v[42:45]
	v_mfma_f32_16x16x32_bf16 v[30:33], v[160:163], v[192:195], v[30:33]
	v_mfma_f32_16x16x32_bf16 v[26:29], v[168:171], v[192:195], v[26:29]
	v_mfma_f32_16x16x32_bf16 v[14:17], v[160:163], v[200:203], v[14:17]
	v_mfma_f32_16x16x32_bf16 v[10:13], v[168:171], v[200:203], v[10:13]
	s_setprio 0
	s_barrier
	s_add_i32 s69, s69, 2
	s_add_u32 s38, s38, 0x100
	s_addc_u32 s39, s39, 0
	s_cmp_gt_u32 s69, 13
	s_cbranch_scc1 .LBB0_209

.LBB0_205:
	s_add_u32 s8, s34, s38
	s_addc_u32 s9, s35, s39
	s_add_u32 s8, s8, 0x100
	s_addc_u32 s9, s9, 0
	s_add_u32 s10, s67, s38
	s_addc_u32 s11, s68, s39
	s_waitcnt lgkmcnt(0)
	s_cmpk_eq_i32 s38, 0x700
	s_cselect_b32 s59, s55, s9
	s_cselect_b32 s58, s54, s8
	s_cselect_b32 s37, s57, s11
	s_cselect_b32 s36, s56, s10
	s_barrier
	s_setprio 1
	s_waitcnt lgkmcnt(0)
	v_mfma_f32_16x16x32_bf16 v[136:139], v[156:159], v[196:199], v[136:139]
	v_mfma_f32_16x16x32_bf16 v[132:135], v[164:167], v[196:199], v[132:135]
	v_mfma_f32_16x16x32_bf16 v[120:123], v[156:159], v[188:191], v[120:123]
	v_mfma_f32_16x16x32_bf16 v[116:119], v[164:167], v[188:191], v[116:119]
	v_mfma_f32_16x16x32_bf16 v[104:107], v[156:159], v[180:183], v[104:107]
	v_mfma_f32_16x16x32_bf16 v[100:103], v[164:167], v[180:183], v[100:103]
	v_mfma_f32_16x16x32_bf16 v[88:91], v[156:159], v[172:175], v[88:91]
	v_mfma_f32_16x16x32_bf16 v[84:87], v[164:167], v[172:175], v[84:87]
	v_mfma_f32_16x16x32_bf16 v[136:139], v[160:163], v[200:203], v[136:139]
	v_mfma_f32_16x16x32_bf16 v[132:135], v[168:171], v[200:203], v[132:135]
	v_mfma_f32_16x16x32_bf16 v[120:123], v[160:163], v[192:195], v[120:123]
	v_mfma_f32_16x16x32_bf16 v[116:119], v[168:171], v[192:195], v[116:119]
	v_mfma_f32_16x16x32_bf16 v[104:107], v[160:163], v[184:187], v[104:107]
	v_mfma_f32_16x16x32_bf16 v[100:103], v[168:171], v[184:187], v[100:103]
	v_mfma_f32_16x16x32_bf16 v[88:91], v[160:163], v[176:179], v[88:91]
	v_mfma_f32_16x16x32_bf16 v[84:87], v[168:171], v[176:179], v[84:87]
	s_setprio 0
	s_setprio 1
	v_mfma_f32_16x16x32_bf16 v[128:131], v[140:143], v[196:199], v[128:131]
	v_mfma_f32_16x16x32_bf16 v[124:127], v[148:151], v[196:199], v[124:127]
	v_mfma_f32_16x16x32_bf16 v[112:115], v[140:143], v[188:191], v[112:115]
	v_mfma_f32_16x16x32_bf16 v[108:111], v[148:151], v[188:191], v[108:111]
	v_mfma_f32_16x16x32_bf16 v[96:99], v[140:143], v[180:183], v[96:99]
	v_mfma_f32_16x16x32_bf16 v[92:95], v[148:151], v[180:183], v[92:95]
	v_mfma_f32_16x16x32_bf16 v[80:83], v[140:143], v[172:175], v[80:83]
	v_mfma_f32_16x16x32_bf16 v[76:79], v[148:151], v[172:175], v[76:79]
	v_mfma_f32_16x16x32_bf16 v[128:131], v[144:147], v[200:203], v[128:131]
	v_mfma_f32_16x16x32_bf16 v[124:127], v[152:155], v[200:203], v[124:127]
	v_mfma_f32_16x16x32_bf16 v[112:115], v[144:147], v[192:195], v[112:115]
	v_mfma_f32_16x16x32_bf16 v[108:111], v[152:155], v[192:195], v[108:111]
	v_mfma_f32_16x16x32_bf16 v[96:99], v[144:147], v[184:187], v[96:99]
	v_mfma_f32_16x16x32_bf16 v[92:95], v[152:155], v[184:187], v[92:95]
	v_mfma_f32_16x16x32_bf16 v[80:83], v[144:147], v[176:179], v[80:83]
	v_mfma_f32_16x16x32_bf16 v[76:79], v[152:155], v[176:179], v[76:79]
	s_setprio 0
	s_barrier
	v_lshl_add_u64 v[234:235], s[36:37], 0, v[210:211]
	s_add_u32 s8, s36, 0x40000
	ds_read_b128 v[196:199], v244 offset:16384
	ds_read_b128 v[200:203], v244 offset:17408
	ds_read_b128 v[188:191], v244 offset:18432
	ds_read_b128 v[192:195], v244 offset:19456
	ds_read_b128 v[180:183], v244 offset:20480
	ds_read_b128 v[184:187], v244 offset:21504
	ds_read_b128 v[172:175], v244 offset:22528
	ds_read_b128 v[176:179], v244 offset:23552
	v_lshl_add_u64 v[232:233], s[36:37], 0, v[214:215]
	s_addc_u32 s9, s37, 0
	v_lshl_add_u64 v[230:231], s[58:59], 0, v[212:213]
	s_mov_b64 s[26:27], -1
	s_and_b64 vcc, exec, s[64:65]
	s_cbranch_vccz .LBB0_207
	s_waitcnt vmcnt(2)
	s_mov_b64 s[26:27], 0
.LBB0_207:
	s_andn2_b64 vcc, exec, s[26:27]
	s_cbranch_vccnz .LBB0_200
	s_waitcnt vmcnt(18)
	s_branch .LBB0_200
